# attention tile loop: static s_setprio 1 for waves 4-7; on top of v25
# baseline (speedup 1.0000x reference)
; __device__ __forceinline__ int v_rd_base(int lane) { return ((lane & 3) << 3) | (((lane >> 2) & 3) << 6) | (((lane >> 4) & 1) << 5) | (((lane >> 5) & 1) << 8); }
; __device__ __forceinline__ void block(const Blk& B, char* lds, A3_LAS unsigned char* ldsl, const int tid) {
;     const int wid = __builtin_amdgcn_readfirstlane(tid >> 6), lane = tid & 63, r32 = lane & 31, hi = lane >> 5;
;     const int NT = (B.P0 + QB3) / 64;
;     char* K_lds = lds + KOFF; char* V_lds = lds + VOFF;
;     float* sc_l = (float*)(lds + SCOFF) + wid * 64;
;     const int vb0 = (int)(uintptr_t)V_lds + attn::v_rd_base(lane);
;     const int qlo = B.P0 + wid * 32, qm = qlo + r32 - 4 * hi;
;     constexpr float C2 = 1.4426950408889634f * attn::SCALE;
;     unsigned kso[2], vso[2];
; #pragma unroll
;     for (int i = 0; i < 2; ++i) { const int row = (2 * wid + i) * 4 + (lane >> 4); const int c = (lane & 15) ^ (row & 7); kso[i] = (unsigned)(row * 128 + c * 8) * 2u; }
; #pragma unroll
;     for (int q = 0; q < 2; ++q) { const int st = 2 * (2 * wid + q) + (lane >> 5), w16 = lane & 31; const int k = (st >> 2) * 8 + (w16 >> 2);
;         const int c = (st & 3) * 32 + (w16 & 3) * 8; vso[q] = (unsigned)(k * 128 + c) * 2u; }
;     ...
;     float m_reg = -1e30f, l_reg = 0.f; bf16x8 qr[8]; f32x16 o[8] = {};
; #pragma unroll
;     for (int d0 = 0; d0 < 8; ++d0) qr[d0] = attn::load8<abf>(B.Q + (size_t)(wid * 32 + r32) * 128 + d0 * 16 + hi * 8);
;     A3_STAGE(0, 0);
;     asm volatile("s_waitcnt vmcnt(0)" ::: "memory");
;     __syncthreads();
.LBB0_323:
	s_cmp_eq_u32 s4, s94
	s_cselect_b32 s6, s95, s93
	s_lshl_b32 s17, s6, 8
	s_lshl_b32 s2, s6, 16
	v_mbcnt_lo_u32_b32 v197, -1, 0
	v_mbcnt_hi_u32_b32 v197, -1, v197
	s_add_u32 s2, s96, s2
	v_add_u32_e32 v0, s33, v197
	s_addc_u32 s3, s97, 0
	v_readfirstlane_b32 s4, v0
	s_ashr_i32 s5, s4, 6
	v_bfe_u32 v0, v197, 4, 2
	s_waitcnt vmcnt(23)
	v_lshl_or_b32 v2, s5, 3, v0
	v_bitop3_b32 v0, v0, v197, 15 bitop3:0x78
	v_lshlrev_b32_e32 v0, 4, v0
	v_and_b32_e32 v3, 15, v197
	v_lshl_or_b32 v199, v2, 8, v0
	v_or_b32_e32 v0, 4, v2
	v_bitop3_b32 v2, v0, v3, 7 bitop3:0x6c
	v_lshlrev_b32_e32 v0, 8, v0
	s_waitcnt vmcnt(21)
	v_lshlrev_b32_e32 v6, 3, v197
	v_lshl_or_b32 v200, v2, 4, v0
	v_and_b32_e32 v0, 24, v6
	v_lshlrev_b32_e32 v2, 5, v197
	v_and_b32_e32 v196, 31, v197
	s_lshl_b32 s56, s5, 5
	v_and_or_b32 v0, v197, 32, v0
	s_lshl_b32 s19, s5, 10
	v_and_b32_e32 v2, 0x380, v2
	v_or3_b32 v0, s19, v2, v0
	v_or_b32_e32 v2, s56, v196
	v_ashrrev_i32_e32 v3, 31, v2
	v_bfe_u32 v198, v197, 5, 1
	v_lshlrev_b64 v[4:5], 8, v[2:3]
	v_lshlrev_b32_e32 v201, 1, v0
	v_lshl_add_u64 v[4:5], s[2:3], 0, v[4:5]
	v_lshlrev_b32_e32 v0, 4, v198
	v_lshl_add_u64 v[4:5], v[4:5], 0, v[0:1]
	s_lshl_b32 s2, s5, 11
	v_or_b32_e32 v202, 0x80, v201
	global_load_dwordx4 v[162:165], v[4:5], off
	global_load_dwordx4 v[166:169], v[4:5], off offset:32
	global_load_dwordx4 v[170:173], v[4:5], off offset:64
	global_load_dwordx4 v[174:177], v[4:5], off offset:96
	global_load_dwordx4 v[178:181], v[4:5], off offset:128
	global_load_dwordx4 v[182:185], v[4:5], off offset:160
	global_load_dwordx4 v[186:189], v[4:5], off offset:192
	global_load_dwordx4 v[190:193], v[4:5], off offset:224
	s_add_i32 s19, s2, 0
	v_mov_b32_e32 v3, v201
	v_mov_b32_e32 v4, v200
	v_mov_b32_e32 v5, v202
	v_mov_b32_e32 v7, v199
	s_mov_b32 m0, s19
	s_and_b32 s3, s4, 0x3fffffc0
	global_load_lds_dwordx4 v7, s[46:47]
	s_add_i32 m0, s19, 0x400
	s_lshl_b32 s3, s3, 2
	global_load_lds_dwordx4 v4, s[46:47]
	s_add_i32 m0, s19, 0x8000
	s_add_i32 s2, s17, 0x100
	global_load_lds_dwordx4 v3, s[48:49]
	s_add_i32 m0, s19, 0xc000
	s_add_i32 s3, s3, 0
	global_load_lds_dwordx4 v3, s[50:51]
	s_add_i32 m0, s19, 0x8400
	s_add_i32 s4, s3, 0x20000
	global_load_lds_dwordx4 v5, s[48:49]
	s_add_i32 m0, s19, 0xc400
	s_add_i32 s23, s56, s17
	global_load_lds_dwordx4 v5, s[50:51]
	s_lshr_b32 s57, s2, 6
	v_lshlrev_b32_e32 v5, 4, v197
	v_lshlrev_b32_e32 v8, 1, v197
	s_movk_i32 s2, 0x70
	v_and_b32_e32 v8, 32, v8
	v_and_b32_e32 v9, 0x70, v5
	v_bitop3_b32 v206, v0, v5, s2 bitop3:0x78
	s_movk_i32 s2, 0x60
	v_lshl_add_u32 v204, v196, 2, s4
	v_add_u32_e32 v203, s4, v0
	s_movk_i32 s4, 0x118
	s_cmp_lg_u32 0, -1
	v_bitop3_b32 v207, v0, v9, 32 bitop3:0x36
	v_bitop3_b32 v208, v0, v9, 64 bitop3:0x36
	v_bitop3_b32 v209, v0, v9, s2 bitop3:0x36
	v_and_or_b32 v0, v6, s4, v8
	s_cselect_b32 s4, 0, 0
	v_and_b32_e32 v3, 63, v197
	v_lshlrev_b32_e32 v4, 2, v198
	v_and_b32_e32 v7, 0xc0, v5
	s_add_i32 s4, s4, 0x8000
	s_waitcnt vmcnt(0)
	v_mov_b32_e32 v14, v1
	v_mov_b32_e32 v15, v1
	s_waitcnt vmcnt(0)
	v_cmp_gt_u32_e64 s[2:3], 32, v3
	v_add3_u32 v210, v7, s4, v0
	v_sub_u32_e32 v211, v2, v4
	v_mov_b32_e32 v0, v1
	v_mov_b32_e32 v2, v1
	v_mov_b32_e32 v3, v1
	v_mov_b32_e32 v4, v1
	v_mov_b32_e32 v5, v1
	v_mov_b32_e32 v6, v1
	v_mov_b32_e32 v7, v1
	v_mov_b32_e32 v8, v1
	v_mov_b32_e32 v9, v1
	v_mov_b32_e32 v10, v1
	v_mov_b32_e32 v11, v1
	v_mov_b32_e32 v12, v1
	v_mov_b32_e32 v13, v1
	v_mov_b64_e32 v[128:129], v[14:15]
	v_mov_b64_e32 v[112:113], v[14:15]
	v_mov_b64_e32 v[96:97], v[14:15]
	v_mov_b64_e32 v[80:81], v[14:15]
	v_mov_b64_e32 v[64:65], v[14:15]
	v_mov_b64_e32 v[48:49], v[14:15]
	v_mov_b64_e32 v[32:33], v[14:15]
	v_mov_b64_e32 v[126:127], v[12:13]
	v_mov_b64_e32 v[124:125], v[10:11]
	v_mov_b64_e32 v[122:123], v[8:9]
	v_mov_b64_e32 v[120:121], v[6:7]
	v_mov_b64_e32 v[118:119], v[4:5]
	v_mov_b64_e32 v[116:117], v[2:3]
	v_mov_b64_e32 v[114:115], v[0:1]
	v_mov_b64_e32 v[110:111], v[12:13]
	v_mov_b64_e32 v[108:109], v[10:11]
	v_mov_b64_e32 v[106:107], v[8:9]
	v_mov_b64_e32 v[104:105], v[6:7]
	v_mov_b64_e32 v[102:103], v[4:5]
	v_mov_b64_e32 v[100:101], v[2:3]
	v_mov_b64_e32 v[98:99], v[0:1]
	v_mov_b64_e32 v[94:95], v[12:13]
	v_mov_b64_e32 v[92:93], v[10:11]
	v_mov_b64_e32 v[90:91], v[8:9]
	v_mov_b64_e32 v[88:89], v[6:7]
	v_mov_b64_e32 v[86:87], v[4:5]
	v_mov_b64_e32 v[84:85], v[2:3]
	v_mov_b64_e32 v[82:83], v[0:1]
	v_mov_b64_e32 v[78:79], v[12:13]
	v_mov_b64_e32 v[76:77], v[10:11]
	v_mov_b64_e32 v[74:75], v[8:9]
	v_mov_b64_e32 v[72:73], v[6:7]
	v_mov_b64_e32 v[70:71], v[4:5]
	v_mov_b64_e32 v[68:69], v[2:3]
	v_mov_b64_e32 v[66:67], v[0:1]
	v_mov_b64_e32 v[62:63], v[12:13]
	v_mov_b64_e32 v[60:61], v[10:11]
	v_mov_b64_e32 v[58:59], v[8:9]
	v_mov_b64_e32 v[56:57], v[6:7]
	v_mov_b64_e32 v[54:55], v[4:5]
	v_mov_b64_e32 v[52:53], v[2:3]
	v_mov_b64_e32 v[50:51], v[0:1]
	v_mov_b64_e32 v[46:47], v[12:13]
	v_mov_b64_e32 v[44:45], v[10:11]
	v_mov_b64_e32 v[42:43], v[8:9]
	v_mov_b64_e32 v[40:41], v[6:7]
	v_mov_b64_e32 v[38:39], v[4:5]
	v_mov_b64_e32 v[36:37], v[2:3]
	v_mov_b64_e32 v[34:35], v[0:1]
	v_mov_b64_e32 v[30:31], v[12:13]
	v_mov_b64_e32 v[28:29], v[10:11]
	v_mov_b64_e32 v[26:27], v[8:9]
	v_mov_b64_e32 v[24:25], v[6:7]
	v_mov_b64_e32 v[22:23], v[4:5]
	v_mov_b64_e32 v[20:21], v[2:3]
	v_mov_b64_e32 v[18:19], v[0:1]
	v_mov_b64_e32 v[16:17], v[14:15]
	s_mov_b32 s5, 1
	v_lshlrev_b32_e32 v205, 8, v196
	v_mov_b32_e32 v212, 0
	v_mov_b32_e32 v213, 0xf149f2ca
	s_movk_i32 s62, 0xff00
	s_mov_b64 s[58:59], s[28:29]
	v_mov_b64_e32 v[14:15], v[12:13]
	v_mov_b64_e32 v[12:13], v[10:11]
	v_mov_b64_e32 v[10:11], v[8:9]
	v_mov_b64_e32 v[8:9], v[6:7]
	v_mov_b64_e32 v[6:7], v[4:5]
	v_mov_b64_e32 v[4:5], v[2:3]
	v_mov_b64_e32 v[2:3], v[0:1]
	s_waitcnt vmcnt(0) lgkmcnt(0)
	s_barrier
	s_mov_b32 s63, 0
	s_cmp_lt_u32 s19, 0x2000
	s_cbranch_scc1 .Latt_noprio
	s_setprio 1
; __device__ __forceinline__ void block(const Blk& B, char* lds, A3_LAS unsigned char* ldsl, const int tid) {
;     ...
;     for (int t = 0; t < NT; ++t) {
;         const int buf = t & 1, kb = t * 64;
;         if (t + 1 < NT) A3_STAGE(t + 1, buf ^ 1);
;         f32x16 p0, p1;
;         attn::qkt<0, false>(p0, p1, K_lds + buf * 16384, r32, hi, qr, true);
.Latt_noprio:
.LBB0_324:
	s_add_i32 s4, s5, -1
	s_and_b32 s20, s4, 1
	s_lshl_b32 s4, s20, 14
	v_add3_u32 v245, s4, v206, v205
	v_add3_u32 v242, s4, v207, v205
	v_add3_u32 v243, s4, v208, v205
	v_add3_u32 v244, s4, v209, v205
	ds_read_b128 v[214:217], v245
	ds_read_b128 v[218:221], v242
	ds_read_b128 v[130:133], v245 offset:8192
	ds_read_b128 v[222:225], v242 offset:8192
	ds_read_b128 v[226:229], v243
	ds_read_b128 v[230:233], v243 offset:8192
	ds_read_b128 v[234:237], v244
	ds_read_b128 v[238:241], v244 offset:8192
	s_cmp_lt_u32 s5, s57
	s_cbranch_scc0 .Latt_x_noload
	s_xor_b32 s21, s4, 0x4000
	s_add_i32 s21, s19, s21
	s_add_i32 s64, s63, 0x8000
	s_cmp_eq_u32 s64, 0x18000
	s_cselect_b32 s64, 0, s64
	s_add_i32 s64, s19, s64
	s_add_u32 s60, s58, s25
	s_addc_u32 s61, s59, s22
	s_mov_b32 m0, s21
	s_nop 0
	global_load_lds_dwordx4 v199, s[60:61]
	s_add_i32 m0, s21, 0x400
	s_nop 0
	global_load_lds_dwordx4 v200, s[60:61]
	s_add_u32 s60, s58, s52
	s_addc_u32 s61, s59, s53
	v_mov_b32_e32 v0, v201
	v_lshl_add_u64 v[146:147], s[60:61], 0, v[0:1]
	v_lshl_add_u64 v[148:149], v[146:147], 0, s[42:43]
	s_add_i32 m0, s64, 0x8000
	v_lshl_add_u64 v[146:147], v[146:147], 0, s[44:45]
	global_load_lds_dwordx4 v[148:149], off
	s_add_i32 m0, s64, 0xc000
	v_mov_b32_e32 v0, v202
	global_load_lds_dwordx4 v[146:147], off
	v_lshl_add_u64 v[146:147], s[60:61], 0, v[0:1]
	v_lshl_add_u64 v[148:149], v[146:147], 0, s[42:43]
	s_add_i32 m0, s64, 0x8400
	v_lshl_add_u64 v[146:147], v[146:147], 0, s[44:45]
	global_load_lds_dwordx4 v[148:149], off
	s_add_i32 m0, s64, 0xc400
	s_nop 0
	global_load_lds_dwordx4 v[146:147], off

; __device__ __forceinline__ int crow(int r, int hi) { return (r & 3) + 8 * (r >> 2) + 4 * hi; }
; __device__ __forceinline__ void block(const Blk& B, char* lds, A3_LAS unsigned char* ldsl, const int tid) {
;     ...
;     { auto rr = __builtin_amdgcn_permlane32_swap(__float_as_uint(l_reg), __float_as_uint(l_reg), false, false); l_reg = __uint_as_float(rr[0]) + __uint_as_float(rr[1]); }
;     if (hi == 0) sc_l[32 + r32] = l_reg;
;     asm volatile("s_waitcnt lgkmcnt(0)" ::: "memory");
;     float rli[16];
; #pragma unroll
;     for (int r = 0; r < 16; ++r) rli[r] = __builtin_amdgcn_rcpf(sc_l[32 + attn::crow(r, hi)]);
;     abf* Ow = B.O + (size_t)(wid * 32) * LDO;
; #pragma unroll
;     for (int r = 0; r < 16; ++r) { const int orow = attn::crow(r, hi);
; #pragma unroll
;         for (int d0 = 0; d0 < 8; ++d0) { const float v = o[d0][r] * rli[r]; const float vn = __shfl_xor(v, 1);
;             if ((r32 & 1) == 0) *(unsigned*)(Ow + (size_t)orow * LDO + d0 * 32 + r32) = attn::cvtpk(v, vn); } }
.LBB0_338:
	s_setprio 0
	v_mov_b32_e32 v0, v146
	s_nop 1
	v_permlane32_swap_b32_e32 v146, v0
	s_and_saveexec_b64 s[58:59], s[2:3]
	v_add_f32_e32 v0, v146, v0
	ds_write_b32 v204, v0 offset:128
	s_or_b64 exec, exec, s[58:59]
	s_waitcnt lgkmcnt(0)
	ds_read_b128 v[142:145], v203 offset:128
	ds_read_b128 v[138:141], v203 offset:160
	ds_read_b128 v[134:137], v203 offset:192
	ds_read_b128 v[130:133], v203 offset:224
	s_lshl_b32 s2, s6, 21
	s_add_u32 s4, s67, s2
	s_addc_u32 s5, s24, 0
	s_ashr_i32 s57, s56, 31
	s_lshl_b64 s[2:3], s[56:57], 13
	s_add_u32 s4, s4, s2
	s_addc_u32 s5, s5, s3
	v_lshlrev_b32_e32 v0, 1, v196
	v_lshl_add_u64 v[146:147], s[4:5], 0, v[0:1]
	v_lshlrev_b32_e32 v0, 15, v198
	v_lshl_add_u64 v[146:147], v[146:147], 0, v[0:1]
	v_and_b32_e32 v0, 1, v197
	v_cmp_eq_u32_e64 s[2:3], 0, v0
	s_waitcnt lgkmcnt(0)
	v_rcp_f32_e32 v142, v142
	v_rcp_f32_e32 v143, v143
	v_rcp_f32_e32 v144, v144
	v_rcp_f32_e32 v145, v145
	v_rcp_f32_e32 v138, v138
	v_rcp_f32_e32 v139, v139
	v_rcp_f32_e32 v140, v140
	v_rcp_f32_e32 v141, v141
	v_rcp_f32_e32 v134, v134
	v_rcp_f32_e32 v135, v135
	v_rcp_f32_e32 v136, v136
	v_rcp_f32_e32 v137, v137
	v_rcp_f32_e32 v130, v130
	v_rcp_f32_e32 v131, v131
	v_rcp_f32_e32 v132, v132
	v_rcp_f32_e32 v133, v133
	s_nop 0
	v_mul_f32_e32 v212, v114, v142
	v_mul_f32_e32 v213, v98, v142
	v_mul_f32_e32 v214, v82, v142
	v_mul_f32_e32 v215, v66, v142
	v_mul_f32_e32 v216, v50, v142
	v_mul_f32_e32 v217, v34, v142
	v_mul_f32_e32 v218, v18, v142
	v_mul_f32_e32 v219, v2, v142
	v_mov_b32_dpp v220, v212 quad_perm:[1,0,3,2] row_mask:0xf bank_mask:0xf
	v_mov_b32_dpp v221, v213 quad_perm:[1,0,3,2] row_mask:0xf bank_mask:0xf
	v_mov_b32_dpp v222, v214 quad_perm:[1,0,3,2] row_mask:0xf bank_mask:0xf
	v_mov_b32_dpp v223, v215 quad_perm:[1,0,3,2] row_mask:0xf bank_mask:0xf
	v_mov_b32_dpp v224, v216 quad_perm:[1,0,3,2] row_mask:0xf bank_mask:0xf
	v_mov_b32_dpp v225, v217 quad_perm:[1,0,3,2] row_mask:0xf bank_mask:0xf
	v_mov_b32_dpp v226, v218 quad_perm:[1,0,3,2] row_mask:0xf bank_mask:0xf
	v_mov_b32_dpp v227, v219 quad_perm:[1,0,3,2] row_mask:0xf bank_mask:0xf
	v_cvt_pk_bf16_f32 v212, v212, v220
	v_cvt_pk_bf16_f32 v213, v213, v221
	v_cvt_pk_bf16_f32 v214, v214, v222
	v_cvt_pk_bf16_f32 v215, v215, v223
	v_cvt_pk_bf16_f32 v216, v216, v224
	v_cvt_pk_bf16_f32 v217, v217, v225
	v_cvt_pk_bf16_f32 v218, v218, v226
	v_cvt_pk_bf16_f32 v219, v219, v227
	s_mov_b64 exec, s[2:3]
	global_store_dword v[146:147], v212, off
	global_store_dword v[146:147], v213, off offset:64
	global_store_dword v[146:147], v214, off offset:128
	global_store_dword v[146:147], v215, off offset:192
	global_store_dword v[146:147], v216, off offset:256
	global_store_dword v[146:147], v217, off offset:320
	global_store_dword v[146:147], v218, off offset:384
	global_store_dword v[146:147], v219, off offset:448
	s_mov_b64 exec, -1
	s_mov_b64 s[60:61], 0x2000
	v_lshl_add_u64 v[228:229], v[146:147], 0, s[60:61]
	v_mul_f32_e32 v230, v115, v143
	v_mul_f32_e32 v231, v99, v143
	v_mul_f32_e32 v232, v83, v143
	v_mul_f32_e32 v233, v67, v143
	v_mul_f32_e32 v234, v51, v143
	v_mul_f32_e32 v235, v35, v143
	v_mul_f32_e32 v236, v19, v143
	v_mul_f32_e32 v237, v3, v143
	v_mov_b32_dpp v238, v230 quad_perm:[1,0,3,2] row_mask:0xf bank_mask:0xf
	v_mov_b32_dpp v239, v231 quad_perm:[1,0,3,2] row_mask:0xf bank_mask:0xf
	v_mov_b32_dpp v240, v232 quad_perm:[1,0,3,2] row_mask:0xf bank_mask:0xf
	v_mov_b32_dpp v241, v233 quad_perm:[1,0,3,2] row_mask:0xf bank_mask:0xf
	v_mov_b32_dpp v242, v234 quad_perm:[1,0,3,2] row_mask:0xf bank_mask:0xf
	v_mov_b32_dpp v243, v235 quad_perm:[1,0,3,2] row_mask:0xf bank_mask:0xf
	v_mov_b32_dpp v244, v236 quad_perm:[1,0,3,2] row_mask:0xf bank_mask:0xf
	v_mov_b32_dpp v245, v237 quad_perm:[1,0,3,2] row_mask:0xf bank_mask:0xf
	v_cvt_pk_bf16_f32 v230, v230, v238
	v_cvt_pk_bf16_f32 v231, v231, v239
	v_cvt_pk_bf16_f32 v232, v232, v240
	v_cvt_pk_bf16_f32 v233, v233, v241
	v_cvt_pk_bf16_f32 v234, v234, v242
	v_cvt_pk_bf16_f32 v235, v235, v243
	v_cvt_pk_bf16_f32 v236, v236, v244
	v_cvt_pk_bf16_f32 v237, v237, v245
	s_mov_b64 exec, s[2:3]
	global_store_dword v[228:229], v230, off
	global_store_dword v[228:229], v231, off offset:64
	global_store_dword v[228:229], v232, off offset:128
	global_store_dword v[228:229], v233, off offset:192
	global_store_dword v[228:229], v234, off offset:256
	global_store_dword v[228:229], v235, off offset:320
	global_store_dword v[228:229], v236, off offset:384
	global_store_dword v[228:229], v237, off offset:448
	s_mov_b64 exec, -1
	s_mov_b64 s[60:61], 0x4000
	v_lshl_add_u64 v[228:229], v[146:147], 0, s[60:61]
	v_mul_f32_e32 v212, v116, v144
	v_mul_f32_e32 v213, v100, v144
	v_mul_f32_e32 v214, v84, v144
	v_mul_f32_e32 v215, v68, v144
	v_mul_f32_e32 v216, v52, v144
	v_mul_f32_e32 v217, v36, v144
	v_mul_f32_e32 v218, v20, v144
	v_mul_f32_e32 v219, v4, v144
	v_mov_b32_dpp v220, v212 quad_perm:[1,0,3,2] row_mask:0xf bank_mask:0xf
	v_mov_b32_dpp v221, v213 quad_perm:[1,0,3,2] row_mask:0xf bank_mask:0xf
	v_mov_b32_dpp v222, v214 quad_perm:[1,0,3,2] row_mask:0xf bank_mask:0xf
	v_mov_b32_dpp v223, v215 quad_perm:[1,0,3,2] row_mask:0xf bank_mask:0xf
	v_mov_b32_dpp v224, v216 quad_perm:[1,0,3,2] row_mask:0xf bank_mask:0xf
	v_mov_b32_dpp v225, v217 quad_perm:[1,0,3,2] row_mask:0xf bank_mask:0xf
	v_mov_b32_dpp v226, v218 quad_perm:[1,0,3,2] row_mask:0xf bank_mask:0xf
	v_mov_b32_dpp v227, v219 quad_perm:[1,0,3,2] row_mask:0xf bank_mask:0xf
	v_cvt_pk_bf16_f32 v212, v212, v220
	v_cvt_pk_bf16_f32 v213, v213, v221
	v_cvt_pk_bf16_f32 v214, v214, v222
	v_cvt_pk_bf16_f32 v215, v215, v223
	v_cvt_pk_bf16_f32 v216, v216, v224
	v_cvt_pk_bf16_f32 v217, v217, v225
	v_cvt_pk_bf16_f32 v218, v218, v226
; __device__ __forceinline__ int crow(int r, int hi) { return (r & 3) + 8 * (r >> 2) + 4 * hi; }
; __device__ __forceinline__ void block(const Blk& B, char* lds, A3_LAS unsigned char* ldsl, const int tid) {
;     ...
;     abf* Ow = B.O + (size_t)(wid * 32) * LDO;
; #pragma unroll
;     for (int r = 0; r < 16; ++r) { const int orow = attn::crow(r, hi);
; #pragma unroll
;         for (int d0 = 0; d0 < 8; ++d0) { const float v = o[d0][r] * rli[r]; const float vn = __shfl_xor(v, 1);
;             if ((r32 & 1) == 0) *(unsigned*)(Ow + (size_t)orow * LDO + d0 * 32 + r32) = attn::cvtpk(v, vn); } }
	v_cvt_pk_bf16_f32 v219, v219, v227
	s_mov_b64 exec, s[2:3]
	global_store_dword v[228:229], v212, off
	global_store_dword v[228:229], v213, off offset:64
	global_store_dword v[228:229], v214, off offset:128
	global_store_dword v[228:229], v215, off offset:192
	global_store_dword v[228:229], v216, off offset:256
	global_store_dword v[228:229], v217, off offset:320
	global_store_dword v[228:229], v218, off offset:384
	global_store_dword v[228:229], v219, off offset:448
	s_mov_b64 exec, -1
	s_mov_b64 s[60:61], 0x6000
	v_lshl_add_u64 v[228:229], v[146:147], 0, s[60:61]
	v_mul_f32_e32 v230, v117, v145
	v_mul_f32_e32 v231, v101, v145
	v_mul_f32_e32 v232, v85, v145
	v_mul_f32_e32 v233, v69, v145
	v_mul_f32_e32 v234, v53, v145
	v_mul_f32_e32 v235, v37, v145
	v_mul_f32_e32 v236, v21, v145
	v_mul_f32_e32 v237, v5, v145
	v_mov_b32_dpp v238, v230 quad_perm:[1,0,3,2] row_mask:0xf bank_mask:0xf
	v_mov_b32_dpp v239, v231 quad_perm:[1,0,3,2] row_mask:0xf bank_mask:0xf
	v_mov_b32_dpp v240, v232 quad_perm:[1,0,3,2] row_mask:0xf bank_mask:0xf
	v_mov_b32_dpp v241, v233 quad_perm:[1,0,3,2] row_mask:0xf bank_mask:0xf
	v_mov_b32_dpp v242, v234 quad_perm:[1,0,3,2] row_mask:0xf bank_mask:0xf
	v_mov_b32_dpp v243, v235 quad_perm:[1,0,3,2] row_mask:0xf bank_mask:0xf
	v_mov_b32_dpp v244, v236 quad_perm:[1,0,3,2] row_mask:0xf bank_mask:0xf
	v_mov_b32_dpp v245, v237 quad_perm:[1,0,3,2] row_mask:0xf bank_mask:0xf
	v_cvt_pk_bf16_f32 v230, v230, v238
	v_cvt_pk_bf16_f32 v231, v231, v239
	v_cvt_pk_bf16_f32 v232, v232, v240
	v_cvt_pk_bf16_f32 v233, v233, v241
	v_cvt_pk_bf16_f32 v234, v234, v242
	v_cvt_pk_bf16_f32 v235, v235, v243
	v_cvt_pk_bf16_f32 v236, v236, v244
	v_cvt_pk_bf16_f32 v237, v237, v245
	s_mov_b64 exec, s[2:3]
	global_store_dword v[228:229], v230, off
	global_store_dword v[228:229], v231, off offset:64
	global_store_dword v[228:229], v232, off offset:128
	global_store_dword v[228:229], v233, off offset:192
	global_store_dword v[228:229], v234, off offset:256
	global_store_dword v[228:229], v235, off offset:320
	global_store_dword v[228:229], v236, off offset:384
	global_store_dword v[228:229], v237, off offset:448
	s_mov_b64 exec, -1
	s_mov_b64 s[60:61], 0x10000
	v_lshl_add_u64 v[228:229], v[146:147], 0, s[60:61]
	v_mul_f32_e32 v212, v118, v138
	v_mul_f32_e32 v213, v102, v138
	v_mul_f32_e32 v214, v86, v138
	v_mul_f32_e32 v215, v70, v138
	v_mul_f32_e32 v216, v54, v138
	v_mul_f32_e32 v217, v38, v138
	v_mul_f32_e32 v218, v22, v138
	v_mul_f32_e32 v219, v6, v138
	v_mov_b32_dpp v220, v212 quad_perm:[1,0,3,2] row_mask:0xf bank_mask:0xf
	v_mov_b32_dpp v221, v213 quad_perm:[1,0,3,2] row_mask:0xf bank_mask:0xf
	v_mov_b32_dpp v222, v214 quad_perm:[1,0,3,2] row_mask:0xf bank_mask:0xf
	v_mov_b32_dpp v223, v215 quad_perm:[1,0,3,2] row_mask:0xf bank_mask:0xf
	v_mov_b32_dpp v224, v216 quad_perm:[1,0,3,2] row_mask:0xf bank_mask:0xf
	v_mov_b32_dpp v225, v217 quad_perm:[1,0,3,2] row_mask:0xf bank_mask:0xf
	v_mov_b32_dpp v226, v218 quad_perm:[1,0,3,2] row_mask:0xf bank_mask:0xf
	v_mov_b32_dpp v227, v219 quad_perm:[1,0,3,2] row_mask:0xf bank_mask:0xf
	v_cvt_pk_bf16_f32 v212, v212, v220
	v_cvt_pk_bf16_f32 v213, v213, v221
	v_cvt_pk_bf16_f32 v214, v214, v222
	v_cvt_pk_bf16_f32 v215, v215, v223
	v_cvt_pk_bf16_f32 v216, v216, v224
	v_cvt_pk_bf16_f32 v217, v217, v225
	v_cvt_pk_bf16_f32 v218, v218, v226
	v_cvt_pk_bf16_f32 v219, v219, v227
	s_mov_b64 exec, s[2:3]
	global_store_dword v[228:229], v212, off
	global_store_dword v[228:229], v213, off offset:64
	global_store_dword v[228:229], v214, off offset:128
	global_store_dword v[228:229], v215, off offset:192
	global_store_dword v[228:229], v216, off offset:256
	global_store_dword v[228:229], v217, off offset:320
	global_store_dword v[228:229], v218, off offset:384
	global_store_dword v[228:229], v219, off offset:448
	s_mov_b64 exec, -1
	s_mov_b64 s[60:61], 0x12000
	v_lshl_add_u64 v[228:229], v[146:147], 0, s[60:61]
	v_mul_f32_e32 v230, v119, v139
	v_mul_f32_e32 v231, v103, v139
	v_mul_f32_e32 v232, v87, v139
	v_mul_f32_e32 v233, v71, v139
	v_mul_f32_e32 v234, v55, v139
	v_mul_f32_e32 v235, v39, v139
	v_mul_f32_e32 v236, v23, v139
	v_mul_f32_e32 v237, v7, v139
	v_mov_b32_dpp v238, v230 quad_perm:[1,0,3,2] row_mask:0xf bank_mask:0xf
	v_mov_b32_dpp v239, v231 quad_perm:[1,0,3,2] row_mask:0xf bank_mask:0xf
	v_mov_b32_dpp v240, v232 quad_perm:[1,0,3,2] row_mask:0xf bank_mask:0xf
	v_mov_b32_dpp v241, v233 quad_perm:[1,0,3,2] row_mask:0xf bank_mask:0xf
	v_mov_b32_dpp v242, v234 quad_perm:[1,0,3,2] row_mask:0xf bank_mask:0xf
	v_mov_b32_dpp v243, v235 quad_perm:[1,0,3,2] row_mask:0xf bank_mask:0xf
	v_mov_b32_dpp v244, v236 quad_perm:[1,0,3,2] row_mask:0xf bank_mask:0xf
	v_mov_b32_dpp v245, v237 quad_perm:[1,0,3,2] row_mask:0xf bank_mask:0xf
	v_cvt_pk_bf16_f32 v230, v230, v238
	v_cvt_pk_bf16_f32 v231, v231, v239
	v_cvt_pk_bf16_f32 v232, v232, v240
	v_cvt_pk_bf16_f32 v233, v233, v241
	v_cvt_pk_bf16_f32 v234, v234, v242
	v_cvt_pk_bf16_f32 v235, v235, v243
	v_cvt_pk_bf16_f32 v236, v236, v244
	v_cvt_pk_bf16_f32 v237, v237, v245
	s_mov_b64 exec, s[2:3]
	global_store_dword v[228:229], v230, off
	global_store_dword v[228:229], v231, off offset:64
	global_store_dword v[228:229], v232, off offset:128
	global_store_dword v[228:229], v233, off offset:192
	global_store_dword v[228:229], v234, off offset:256
	global_store_dword v[228:229], v235, off offset:320
	global_store_dword v[228:229], v236, off offset:384
	global_store_dword v[228:229], v237, off offset:448
	s_mov_b64 exec, -1
	s_mov_b64 s[60:61], 0x14000
	v_lshl_add_u64 v[228:229], v[146:147], 0, s[60:61]
	v_mul_f32_e32 v212, v120, v140
	v_mul_f32_e32 v213, v104, v140
	v_mul_f32_e32 v214, v88, v140
; __device__ __forceinline__ int crow(int r, int hi) { return (r & 3) + 8 * (r >> 2) + 4 * hi; }
; __device__ __forceinline__ void block(const Blk& B, char* lds, A3_LAS unsigned char* ldsl, const int tid) {
;     ...
;     abf* Ow = B.O + (size_t)(wid * 32) * LDO;
; #pragma unroll
;     for (int r = 0; r < 16; ++r) { const int orow = attn::crow(r, hi);
; #pragma unroll
;         for (int d0 = 0; d0 < 8; ++d0) { const float v = o[d0][r] * rli[r]; const float vn = __shfl_xor(v, 1);
;             if ((r32 & 1) == 0) *(unsigned*)(Ow + (size_t)orow * LDO + d0 * 32 + r32) = attn::cvtpk(v, vn); } }
	v_mul_f32_e32 v215, v72, v140
	v_mul_f32_e32 v216, v56, v140
	v_mul_f32_e32 v217, v40, v140
	v_mul_f32_e32 v218, v24, v140
	v_mul_f32_e32 v219, v8, v140
	v_mov_b32_dpp v220, v212 quad_perm:[1,0,3,2] row_mask:0xf bank_mask:0xf
	v_mov_b32_dpp v221, v213 quad_perm:[1,0,3,2] row_mask:0xf bank_mask:0xf
	v_mov_b32_dpp v222, v214 quad_perm:[1,0,3,2] row_mask:0xf bank_mask:0xf
	v_mov_b32_dpp v223, v215 quad_perm:[1,0,3,2] row_mask:0xf bank_mask:0xf
	v_mov_b32_dpp v224, v216 quad_perm:[1,0,3,2] row_mask:0xf bank_mask:0xf
	v_mov_b32_dpp v225, v217 quad_perm:[1,0,3,2] row_mask:0xf bank_mask:0xf
	v_mov_b32_dpp v226, v218 quad_perm:[1,0,3,2] row_mask:0xf bank_mask:0xf
	v_mov_b32_dpp v227, v219 quad_perm:[1,0,3,2] row_mask:0xf bank_mask:0xf
	v_cvt_pk_bf16_f32 v212, v212, v220
	v_cvt_pk_bf16_f32 v213, v213, v221
	v_cvt_pk_bf16_f32 v214, v214, v222
	v_cvt_pk_bf16_f32 v215, v215, v223
	v_cvt_pk_bf16_f32 v216, v216, v224
	v_cvt_pk_bf16_f32 v217, v217, v225
	v_cvt_pk_bf16_f32 v218, v218, v226
	v_cvt_pk_bf16_f32 v219, v219, v227
	s_mov_b64 exec, s[2:3]
	global_store_dword v[228:229], v212, off
	global_store_dword v[228:229], v213, off offset:64
	global_store_dword v[228:229], v214, off offset:128
	global_store_dword v[228:229], v215, off offset:192
	global_store_dword v[228:229], v216, off offset:256
	global_store_dword v[228:229], v217, off offset:320
	global_store_dword v[228:229], v218, off offset:384
	global_store_dword v[228:229], v219, off offset:448
	s_mov_b64 exec, -1
	s_mov_b64 s[60:61], 0x16000
	v_lshl_add_u64 v[228:229], v[146:147], 0, s[60:61]
	v_mul_f32_e32 v230, v121, v141
	v_mul_f32_e32 v231, v105, v141
	v_mul_f32_e32 v232, v89, v141
	v_mul_f32_e32 v233, v73, v141
	v_mul_f32_e32 v234, v57, v141
	v_mul_f32_e32 v235, v41, v141
	v_mul_f32_e32 v236, v25, v141
	v_mul_f32_e32 v237, v9, v141
	v_mov_b32_dpp v238, v230 quad_perm:[1,0,3,2] row_mask:0xf bank_mask:0xf
	v_mov_b32_dpp v239, v231 quad_perm:[1,0,3,2] row_mask:0xf bank_mask:0xf
	v_mov_b32_dpp v240, v232 quad_perm:[1,0,3,2] row_mask:0xf bank_mask:0xf
	v_mov_b32_dpp v241, v233 quad_perm:[1,0,3,2] row_mask:0xf bank_mask:0xf
	v_mov_b32_dpp v242, v234 quad_perm:[1,0,3,2] row_mask:0xf bank_mask:0xf
	v_mov_b32_dpp v243, v235 quad_perm:[1,0,3,2] row_mask:0xf bank_mask:0xf
	v_mov_b32_dpp v244, v236 quad_perm:[1,0,3,2] row_mask:0xf bank_mask:0xf
	v_mov_b32_dpp v245, v237 quad_perm:[1,0,3,2] row_mask:0xf bank_mask:0xf
	v_cvt_pk_bf16_f32 v230, v230, v238
	v_cvt_pk_bf16_f32 v231, v231, v239
	v_cvt_pk_bf16_f32 v232, v232, v240
	v_cvt_pk_bf16_f32 v233, v233, v241
	v_cvt_pk_bf16_f32 v234, v234, v242
	v_cvt_pk_bf16_f32 v235, v235, v243
	v_cvt_pk_bf16_f32 v236, v236, v244
	v_cvt_pk_bf16_f32 v237, v237, v245
	s_mov_b64 exec, s[2:3]
	global_store_dword v[228:229], v230, off
	global_store_dword v[228:229], v231, off offset:64
	global_store_dword v[228:229], v232, off offset:128
	global_store_dword v[228:229], v233, off offset:192
	global_store_dword v[228:229], v234, off offset:256
	global_store_dword v[228:229], v235, off offset:320
	global_store_dword v[228:229], v236, off offset:384
	global_store_dword v[228:229], v237, off offset:448
	s_mov_b64 exec, -1
	s_mov_b64 s[60:61], 0x20000
	v_lshl_add_u64 v[228:229], v[146:147], 0, s[60:61]
	v_mul_f32_e32 v212, v122, v134
	v_mul_f32_e32 v213, v106, v134
	v_mul_f32_e32 v214, v90, v134
	v_mul_f32_e32 v215, v74, v134
	v_mul_f32_e32 v216, v58, v134
	v_mul_f32_e32 v217, v42, v134
	v_mul_f32_e32 v218, v26, v134
	v_mul_f32_e32 v219, v10, v134
	v_mov_b32_dpp v220, v212 quad_perm:[1,0,3,2] row_mask:0xf bank_mask:0xf
	v_mov_b32_dpp v221, v213 quad_perm:[1,0,3,2] row_mask:0xf bank_mask:0xf
	v_mov_b32_dpp v222, v214 quad_perm:[1,0,3,2] row_mask:0xf bank_mask:0xf
	v_mov_b32_dpp v223, v215 quad_perm:[1,0,3,2] row_mask:0xf bank_mask:0xf
	v_mov_b32_dpp v224, v216 quad_perm:[1,0,3,2] row_mask:0xf bank_mask:0xf
	v_mov_b32_dpp v225, v217 quad_perm:[1,0,3,2] row_mask:0xf bank_mask:0xf
	v_mov_b32_dpp v226, v218 quad_perm:[1,0,3,2] row_mask:0xf bank_mask:0xf
	v_mov_b32_dpp v227, v219 quad_perm:[1,0,3,2] row_mask:0xf bank_mask:0xf
	v_cvt_pk_bf16_f32 v212, v212, v220
	v_cvt_pk_bf16_f32 v213, v213, v221
	v_cvt_pk_bf16_f32 v214, v214, v222
	v_cvt_pk_bf16_f32 v215, v215, v223
	v_cvt_pk_bf16_f32 v216, v216, v224
	v_cvt_pk_bf16_f32 v217, v217, v225
	v_cvt_pk_bf16_f32 v218, v218, v226
	v_cvt_pk_bf16_f32 v219, v219, v227
	s_mov_b64 exec, s[2:3]
	global_store_dword v[228:229], v212, off
	global_store_dword v[228:229], v213, off offset:64
	global_store_dword v[228:229], v214, off offset:128
	global_store_dword v[228:229], v215, off offset:192
	global_store_dword v[228:229], v216, off offset:256
	global_store_dword v[228:229], v217, off offset:320
	global_store_dword v[228:229], v218, off offset:384
	global_store_dword v[228:229], v219, off offset:448
	s_mov_b64 exec, -1
	s_mov_b64 s[60:61], 0x22000
	v_lshl_add_u64 v[228:229], v[146:147], 0, s[60:61]
	v_mul_f32_e32 v230, v123, v135
	v_mul_f32_e32 v231, v107, v135
	v_mul_f32_e32 v232, v91, v135
	v_mul_f32_e32 v233, v75, v135
	v_mul_f32_e32 v234, v59, v135
	v_mul_f32_e32 v235, v43, v135
	v_mul_f32_e32 v236, v27, v135
	v_mul_f32_e32 v237, v11, v135
	v_mov_b32_dpp v238, v230 quad_perm:[1,0,3,2] row_mask:0xf bank_mask:0xf
	v_mov_b32_dpp v239, v231 quad_perm:[1,0,3,2] row_mask:0xf bank_mask:0xf
	v_mov_b32_dpp v240, v232 quad_perm:[1,0,3,2] row_mask:0xf bank_mask:0xf
	v_mov_b32_dpp v241, v233 quad_perm:[1,0,3,2] row_mask:0xf bank_mask:0xf
	v_mov_b32_dpp v242, v234 quad_perm:[1,0,3,2] row_mask:0xf bank_mask:0xf
	v_mov_b32_dpp v243, v235 quad_perm:[1,0,3,2] row_mask:0xf bank_mask:0xf
	v_mov_b32_dpp v244, v236 quad_perm:[1,0,3,2] row_mask:0xf bank_mask:0xf
; __device__ __forceinline__ int crow(int r, int hi) { return (r & 3) + 8 * (r >> 2) + 4 * hi; }
; __device__ __forceinline__ void block(const Blk& B, char* lds, A3_LAS unsigned char* ldsl, const int tid) {
;     ...
;     abf* Ow = B.O + (size_t)(wid * 32) * LDO;
; #pragma unroll
;     for (int r = 0; r < 16; ++r) { const int orow = attn::crow(r, hi);
; #pragma unroll
;         for (int d0 = 0; d0 < 8; ++d0) { const float v = o[d0][r] * rli[r]; const float vn = __shfl_xor(v, 1);
;             if ((r32 & 1) == 0) *(unsigned*)(Ow + (size_t)orow * LDO + d0 * 32 + r32) = attn::cvtpk(v, vn); } }
	v_mov_b32_dpp v245, v237 quad_perm:[1,0,3,2] row_mask:0xf bank_mask:0xf
	v_cvt_pk_bf16_f32 v230, v230, v238
	v_cvt_pk_bf16_f32 v231, v231, v239
	v_cvt_pk_bf16_f32 v232, v232, v240
	v_cvt_pk_bf16_f32 v233, v233, v241
	v_cvt_pk_bf16_f32 v234, v234, v242
	v_cvt_pk_bf16_f32 v235, v235, v243
	v_cvt_pk_bf16_f32 v236, v236, v244
	v_cvt_pk_bf16_f32 v237, v237, v245
	s_mov_b64 exec, s[2:3]
	global_store_dword v[228:229], v230, off
	global_store_dword v[228:229], v231, off offset:64
	global_store_dword v[228:229], v232, off offset:128
	global_store_dword v[228:229], v233, off offset:192
	global_store_dword v[228:229], v234, off offset:256
	global_store_dword v[228:229], v235, off offset:320
	global_store_dword v[228:229], v236, off offset:384
	global_store_dword v[228:229], v237, off offset:448
	s_mov_b64 exec, -1
	s_mov_b64 s[60:61], 0x24000
	v_lshl_add_u64 v[228:229], v[146:147], 0, s[60:61]
	v_mul_f32_e32 v212, v124, v136
	v_mul_f32_e32 v213, v108, v136
	v_mul_f32_e32 v214, v92, v136
	v_mul_f32_e32 v215, v76, v136
	v_mul_f32_e32 v216, v60, v136
	v_mul_f32_e32 v217, v44, v136
	v_mul_f32_e32 v218, v28, v136
	v_mul_f32_e32 v219, v12, v136
	v_mov_b32_dpp v220, v212 quad_perm:[1,0,3,2] row_mask:0xf bank_mask:0xf
	v_mov_b32_dpp v221, v213 quad_perm:[1,0,3,2] row_mask:0xf bank_mask:0xf
	v_mov_b32_dpp v222, v214 quad_perm:[1,0,3,2] row_mask:0xf bank_mask:0xf
	v_mov_b32_dpp v223, v215 quad_perm:[1,0,3,2] row_mask:0xf bank_mask:0xf
	v_mov_b32_dpp v224, v216 quad_perm:[1,0,3,2] row_mask:0xf bank_mask:0xf
	v_mov_b32_dpp v225, v217 quad_perm:[1,0,3,2] row_mask:0xf bank_mask:0xf
	v_mov_b32_dpp v226, v218 quad_perm:[1,0,3,2] row_mask:0xf bank_mask:0xf
	v_mov_b32_dpp v227, v219 quad_perm:[1,0,3,2] row_mask:0xf bank_mask:0xf
	v_cvt_pk_bf16_f32 v212, v212, v220
	v_cvt_pk_bf16_f32 v213, v213, v221
	v_cvt_pk_bf16_f32 v214, v214, v222
	v_cvt_pk_bf16_f32 v215, v215, v223
	v_cvt_pk_bf16_f32 v216, v216, v224
	v_cvt_pk_bf16_f32 v217, v217, v225
	v_cvt_pk_bf16_f32 v218, v218, v226
	v_cvt_pk_bf16_f32 v219, v219, v227
	s_mov_b64 exec, s[2:3]
	global_store_dword v[228:229], v212, off
	global_store_dword v[228:229], v213, off offset:64
	global_store_dword v[228:229], v214, off offset:128
	global_store_dword v[228:229], v215, off offset:192
	global_store_dword v[228:229], v216, off offset:256
	global_store_dword v[228:229], v217, off offset:320
	global_store_dword v[228:229], v218, off offset:384
	global_store_dword v[228:229], v219, off offset:448
	s_mov_b64 exec, -1
	s_mov_b64 s[60:61], 0x26000
	v_lshl_add_u64 v[228:229], v[146:147], 0, s[60:61]
	v_mul_f32_e32 v230, v125, v137
	v_mul_f32_e32 v231, v109, v137
	v_mul_f32_e32 v232, v93, v137
	v_mul_f32_e32 v233, v77, v137
	v_mul_f32_e32 v234, v61, v137
	v_mul_f32_e32 v235, v45, v137
	v_mul_f32_e32 v236, v29, v137
	v_mul_f32_e32 v237, v13, v137
	v_mov_b32_dpp v238, v230 quad_perm:[1,0,3,2] row_mask:0xf bank_mask:0xf
	v_mov_b32_dpp v239, v231 quad_perm:[1,0,3,2] row_mask:0xf bank_mask:0xf
	v_mov_b32_dpp v240, v232 quad_perm:[1,0,3,2] row_mask:0xf bank_mask:0xf
	v_mov_b32_dpp v241, v233 quad_perm:[1,0,3,2] row_mask:0xf bank_mask:0xf
	v_mov_b32_dpp v242, v234 quad_perm:[1,0,3,2] row_mask:0xf bank_mask:0xf
	v_mov_b32_dpp v243, v235 quad_perm:[1,0,3,2] row_mask:0xf bank_mask:0xf
	v_mov_b32_dpp v244, v236 quad_perm:[1,0,3,2] row_mask:0xf bank_mask:0xf
	v_mov_b32_dpp v245, v237 quad_perm:[1,0,3,2] row_mask:0xf bank_mask:0xf
	v_cvt_pk_bf16_f32 v230, v230, v238
	v_cvt_pk_bf16_f32 v231, v231, v239
	v_cvt_pk_bf16_f32 v232, v232, v240
	v_cvt_pk_bf16_f32 v233, v233, v241
	v_cvt_pk_bf16_f32 v234, v234, v242
	v_cvt_pk_bf16_f32 v235, v235, v243
	v_cvt_pk_bf16_f32 v236, v236, v244
	v_cvt_pk_bf16_f32 v237, v237, v245
	s_mov_b64 exec, s[2:3]
	global_store_dword v[228:229], v230, off
	global_store_dword v[228:229], v231, off offset:64
	global_store_dword v[228:229], v232, off offset:128
	global_store_dword v[228:229], v233, off offset:192
	global_store_dword v[228:229], v234, off offset:256
	global_store_dword v[228:229], v235, off offset:320
	global_store_dword v[228:229], v236, off offset:384
	global_store_dword v[228:229], v237, off offset:448
	s_mov_b64 exec, -1
	s_mov_b64 s[60:61], 0x30000
	v_lshl_add_u64 v[228:229], v[146:147], 0, s[60:61]
	v_mul_f32_e32 v212, v126, v130
	v_mul_f32_e32 v213, v110, v130
	v_mul_f32_e32 v214, v94, v130
	v_mul_f32_e32 v215, v78, v130
	v_mul_f32_e32 v216, v62, v130
	v_mul_f32_e32 v217, v46, v130
	v_mul_f32_e32 v218, v30, v130
	v_mul_f32_e32 v219, v14, v130
	v_mov_b32_dpp v220, v212 quad_perm:[1,0,3,2] row_mask:0xf bank_mask:0xf
	v_mov_b32_dpp v221, v213 quad_perm:[1,0,3,2] row_mask:0xf bank_mask:0xf
	v_mov_b32_dpp v222, v214 quad_perm:[1,0,3,2] row_mask:0xf bank_mask:0xf
	v_mov_b32_dpp v223, v215 quad_perm:[1,0,3,2] row_mask:0xf bank_mask:0xf
	v_mov_b32_dpp v224, v216 quad_perm:[1,0,3,2] row_mask:0xf bank_mask:0xf
	v_mov_b32_dpp v225, v217 quad_perm:[1,0,3,2] row_mask:0xf bank_mask:0xf
	v_mov_b32_dpp v226, v218 quad_perm:[1,0,3,2] row_mask:0xf bank_mask:0xf
	v_mov_b32_dpp v227, v219 quad_perm:[1,0,3,2] row_mask:0xf bank_mask:0xf
	v_cvt_pk_bf16_f32 v212, v212, v220
	v_cvt_pk_bf16_f32 v213, v213, v221
	v_cvt_pk_bf16_f32 v214, v214, v222
	v_cvt_pk_bf16_f32 v215, v215, v223
	v_cvt_pk_bf16_f32 v216, v216, v224
	v_cvt_pk_bf16_f32 v217, v217, v225
	v_cvt_pk_bf16_f32 v218, v218, v226
	v_cvt_pk_bf16_f32 v219, v219, v227
	s_mov_b64 exec, s[2:3]
	global_store_dword v[228:229], v212, off
	global_store_dword v[228:229], v213, off offset:64
	global_store_dword v[228:229], v214, off offset:128
	global_store_dword v[228:229], v215, off offset:192
	global_store_dword v[228:229], v216, off offset:256
; __device__ __forceinline__ int crow(int r, int hi) { return (r & 3) + 8 * (r >> 2) + 4 * hi; }
; #define LAS __attribute__((address_space(3)))
; __device__ __forceinline__ int fresh_lane() { int l; asm volatile("v_mbcnt_lo_u32_b32 %0, -1, 0\n\tv_mbcnt_hi_u32_b32 %0, -1, %0" : "=v"(l)); return l; }
; __device__ __forceinline__ KP kargs() { KP kp = (KP)__builtin_amdgcn_kernarg_segment_ptr(); asm volatile("" : "+s"(kp)); return kp; }
; __device__ __forceinline__ void block(const Blk& B, char* lds, A3_LAS unsigned char* ldsl, const int tid) {
;     ...
;     abf* Ow = B.O + (size_t)(wid * 32) * LDO;
; #pragma unroll
;     for (int r = 0; r < 16; ++r) { const int orow = attn::crow(r, hi);
; #pragma unroll
;         for (int d0 = 0; d0 < 8; ++d0) { const float v = o[d0][r] * rli[r]; const float vn = __shfl_xor(v, 1);
;             if ((r32 & 1) == 0) *(unsigned*)(Ow + (size_t)orow * LDO + d0 * 32 + r32) = attn::cvtpk(v, vn); } }
;     __syncthreads();
; __device__ __forceinline__ void phase3(KP kp, char* lds, LAS unsigned char* ldsl, int wave, int bid, int G) {
;     ...
;         for (int pass = 0; pass < 2; ++pass) {
;             const int qb = (pass ^ ((y ^ j) & 1)) ? y : 31 - y;
;             attn3::Blk B; B.Q = Qb + ((size_t)j * T + (size_t)qb * 256) * 128; B.K = Kb + (size_t)j * T * 128;
;             B.V0 = Vb + (size_t)((j >> 1) * 2) * T * 128; B.V1 = B.V0 + (size_t)T * 128;
;             B.O = OAp + (size_t)(qb * 256) * 4096 + j * 256; B.P0 = qb * 256;
;             const int tid_p = wave * 64 + fresh_lane();
;             attn3::block(B, lds, ldsl, tid_p);
;             if (pass == 0) { conv_run(kargs(), KWS(), (LAS unsigned*)(ldsl + wave * 8320), fresh_lane(), CONV_DENSE_ITEMS + bid * NWAVES + wave, CONV_UP_END, G * NWAVES); __syncthreads(); }
;         }
	global_store_dword v[228:229], v217, off offset:320
	global_store_dword v[228:229], v218, off offset:384
	global_store_dword v[228:229], v219, off offset:448
	s_mov_b64 exec, -1
	s_mov_b64 s[60:61], 0x32000
	v_lshl_add_u64 v[228:229], v[146:147], 0, s[60:61]
	v_mul_f32_e32 v230, v127, v131
	v_mul_f32_e32 v231, v111, v131
	v_mul_f32_e32 v232, v95, v131
	v_mul_f32_e32 v233, v79, v131
	v_mul_f32_e32 v234, v63, v131
	v_mul_f32_e32 v235, v47, v131
	v_mul_f32_e32 v236, v31, v131
	v_mul_f32_e32 v237, v15, v131
	v_mov_b32_dpp v238, v230 quad_perm:[1,0,3,2] row_mask:0xf bank_mask:0xf
	v_mov_b32_dpp v239, v231 quad_perm:[1,0,3,2] row_mask:0xf bank_mask:0xf
	v_mov_b32_dpp v240, v232 quad_perm:[1,0,3,2] row_mask:0xf bank_mask:0xf
	v_mov_b32_dpp v241, v233 quad_perm:[1,0,3,2] row_mask:0xf bank_mask:0xf
	v_mov_b32_dpp v242, v234 quad_perm:[1,0,3,2] row_mask:0xf bank_mask:0xf
	v_mov_b32_dpp v243, v235 quad_perm:[1,0,3,2] row_mask:0xf bank_mask:0xf
	v_mov_b32_dpp v244, v236 quad_perm:[1,0,3,2] row_mask:0xf bank_mask:0xf
	v_mov_b32_dpp v245, v237 quad_perm:[1,0,3,2] row_mask:0xf bank_mask:0xf
	v_cvt_pk_bf16_f32 v230, v230, v238
	v_cvt_pk_bf16_f32 v231, v231, v239
	v_cvt_pk_bf16_f32 v232, v232, v240
	v_cvt_pk_bf16_f32 v233, v233, v241
	v_cvt_pk_bf16_f32 v234, v234, v242
	v_cvt_pk_bf16_f32 v235, v235, v243
	v_cvt_pk_bf16_f32 v236, v236, v244
	v_cvt_pk_bf16_f32 v237, v237, v245
	s_mov_b64 exec, s[2:3]
	global_store_dword v[228:229], v230, off
	global_store_dword v[228:229], v231, off offset:64
	global_store_dword v[228:229], v232, off offset:128
	global_store_dword v[228:229], v233, off offset:192
	global_store_dword v[228:229], v234, off offset:256
	global_store_dword v[228:229], v235, off offset:320
	global_store_dword v[228:229], v236, off offset:384
	global_store_dword v[228:229], v237, off offset:448
	s_mov_b64 exec, -1
	s_mov_b64 s[60:61], 0x34000
	v_lshl_add_u64 v[228:229], v[146:147], 0, s[60:61]
	v_mul_f32_e32 v212, v128, v132
	v_mul_f32_e32 v213, v112, v132
	v_mul_f32_e32 v214, v96, v132
	v_mul_f32_e32 v215, v80, v132
	v_mul_f32_e32 v216, v64, v132
	v_mul_f32_e32 v217, v48, v132
	v_mul_f32_e32 v218, v32, v132
	v_mul_f32_e32 v219, v16, v132
	v_mov_b32_dpp v220, v212 quad_perm:[1,0,3,2] row_mask:0xf bank_mask:0xf
	v_mov_b32_dpp v221, v213 quad_perm:[1,0,3,2] row_mask:0xf bank_mask:0xf
	v_mov_b32_dpp v222, v214 quad_perm:[1,0,3,2] row_mask:0xf bank_mask:0xf
	v_mov_b32_dpp v223, v215 quad_perm:[1,0,3,2] row_mask:0xf bank_mask:0xf
	v_mov_b32_dpp v224, v216 quad_perm:[1,0,3,2] row_mask:0xf bank_mask:0xf
	v_mov_b32_dpp v225, v217 quad_perm:[1,0,3,2] row_mask:0xf bank_mask:0xf
	v_mov_b32_dpp v226, v218 quad_perm:[1,0,3,2] row_mask:0xf bank_mask:0xf
	v_mov_b32_dpp v227, v219 quad_perm:[1,0,3,2] row_mask:0xf bank_mask:0xf
	v_cvt_pk_bf16_f32 v212, v212, v220
	v_cvt_pk_bf16_f32 v213, v213, v221
	v_cvt_pk_bf16_f32 v214, v214, v222
	v_cvt_pk_bf16_f32 v215, v215, v223
	v_cvt_pk_bf16_f32 v216, v216, v224
	v_cvt_pk_bf16_f32 v217, v217, v225
	v_cvt_pk_bf16_f32 v218, v218, v226
	v_cvt_pk_bf16_f32 v219, v219, v227
	s_mov_b64 exec, s[2:3]
	global_store_dword v[228:229], v212, off
	global_store_dword v[228:229], v213, off offset:64
	global_store_dword v[228:229], v214, off offset:128
	global_store_dword v[228:229], v215, off offset:192
	global_store_dword v[228:229], v216, off offset:256
	global_store_dword v[228:229], v217, off offset:320
	global_store_dword v[228:229], v218, off offset:384
	global_store_dword v[228:229], v219, off offset:448
	s_mov_b64 exec, -1
	s_mov_b64 s[60:61], 0x36000
	v_lshl_add_u64 v[228:229], v[146:147], 0, s[60:61]
	v_mul_f32_e32 v230, v129, v133
	v_mul_f32_e32 v231, v113, v133
	v_mul_f32_e32 v232, v97, v133
	v_mul_f32_e32 v233, v81, v133
	v_mul_f32_e32 v234, v65, v133
	v_mul_f32_e32 v235, v49, v133
	v_mul_f32_e32 v236, v33, v133
	v_mul_f32_e32 v237, v17, v133
	v_mov_b32_dpp v238, v230 quad_perm:[1,0,3,2] row_mask:0xf bank_mask:0xf
	v_mov_b32_dpp v239, v231 quad_perm:[1,0,3,2] row_mask:0xf bank_mask:0xf
	v_mov_b32_dpp v240, v232 quad_perm:[1,0,3,2] row_mask:0xf bank_mask:0xf
	v_mov_b32_dpp v241, v233 quad_perm:[1,0,3,2] row_mask:0xf bank_mask:0xf
	v_mov_b32_dpp v242, v234 quad_perm:[1,0,3,2] row_mask:0xf bank_mask:0xf
	v_mov_b32_dpp v243, v235 quad_perm:[1,0,3,2] row_mask:0xf bank_mask:0xf
	v_mov_b32_dpp v244, v236 quad_perm:[1,0,3,2] row_mask:0xf bank_mask:0xf
	v_mov_b32_dpp v245, v237 quad_perm:[1,0,3,2] row_mask:0xf bank_mask:0xf
	v_cvt_pk_bf16_f32 v230, v230, v238
	v_cvt_pk_bf16_f32 v231, v231, v239
	v_cvt_pk_bf16_f32 v232, v232, v240
	v_cvt_pk_bf16_f32 v233, v233, v241
	v_cvt_pk_bf16_f32 v234, v234, v242
	v_cvt_pk_bf16_f32 v235, v235, v243
	v_cvt_pk_bf16_f32 v236, v236, v244
	v_cvt_pk_bf16_f32 v237, v237, v245
	s_mov_b64 exec, s[2:3]
	global_store_dword v[228:229], v230, off
	global_store_dword v[228:229], v231, off offset:64
	global_store_dword v[228:229], v232, off offset:128
	global_store_dword v[228:229], v233, off offset:192
	global_store_dword v[228:229], v234, off offset:256
	global_store_dword v[228:229], v235, off offset:320
	global_store_dword v[228:229], v236, off offset:384
	global_store_dword v[228:229], v237, off offset:448
	s_mov_b64 exec, -1
	s_andn2_b64 vcc, exec, s[54:55]
	s_mov_b64 s[2:3], -1
	s_waitcnt lgkmcnt(0)
	s_barrier
	s_cbranch_vccnz .LBB0_322
	s_mov_b64 s[2:3], s[0:1]
	s_andn2_b64 vcc, exec, s[8:9]
	v_mbcnt_lo_u32_b32 v66, -1, 0
	v_mbcnt_hi_u32_b32 v66, -1, v66
	s_cbranch_vccnz .LBB0_321
	s_mov_b64 s[58:59], -1
	s_and_b64 vcc, exec, s[10:11]
	s_cbranch_vccz .LBB0_611
	s_and_b64 vcc, exec, s[12:13]
	s_cbranch_vccz .LBB0_608
	s_and_b64 vcc, exec, s[14:15]
	s_cbranch_vccz .LBB0_606
	s_mov_b64 s[54:55], -1
	s_and_b64 vcc, exec, s[26:27]
	s_cbranch_vccz .LBB0_603
	s_load_dwordx2 s[4:5], s[2:3], 0x98
	s_mov_b64 s[54:55], 0
	s_waitcnt lgkmcnt(0)
	s_add_u32 s56, s4, s30
	s_addc_u32 s57, s5, s31
